# static s_setprio 1 for waves 0-3 during the c3 chunk loop, on top of c3 counted waits + mixer rewrite + flat release
# speedup vs baseline: 1.0028x; 1.0028x over previous
.LBB0_658:
	v_writelane_b32 v247, s23, 38
	s_andn2_b64 vcc, exec, s[8:9]
	v_writelane_b32 v247, s91, 39
	s_cbranch_vccnz .LBB0_709
	v_readlane_b32 s0, v247, 36
	v_readlane_b32 s1, v247, 37
	s_lshl_b32 s66, s0, 7
	s_lshl_b64 s[0:1], s[66:67], 2
	s_add_u32 s0, s12, s0
	s_addc_u32 s1, s11, s1
	s_lshl_b32 s5, s4, 4
	s_cmp_gt_u32 s49, 1
	v_lshlrev_b32_e32 v36, 4, v35
	s_cselect_b64 s[94:95], -1, 0
	v_ashrrev_i32_e32 v104, 3, v35
	v_and_b32_e32 v36, 0x70, v36
	s_movk_i32 s11, 0x90
	s_and_b64 s[2:3], s[94:95], exec
	v_mad_u64_u32 v[90:91], s[2:3], v104, s11, v[36:37]
	s_cselect_b32 s64, 6, 0
	s_lshl_b32 s8, s4, 5
	v_lshlrev_b32_e32 v40, 3, v35
	s_ashr_i32 s2, s5, 31
	s_add_i32 s9, s8, 0
	v_lshl_add_u32 v37, v104, 1, 0
	v_and_b32_e32 v92, 0x78, v40
	v_and_b32_e32 v43, 15, v35
	v_mov_b32_e32 v41, s2
	s_ashr_i32 s2, s10, 3
	s_add_i32 s9, s9, 0x14800
	v_mul_u32_u24_e32 v39, 0x90, v36
	v_mad_u32_u24 v91, v36, s11, v37
	v_mov_b32_e32 v36, s5
	v_or_b32_e32 v40, s5, v43
	s_ashr_i32 s5, s4, 31
	s_and_b32 s3, s2, -16
	v_lshl_add_u32 v53, v43, 1, s9
	s_lshl_b32 s9, s4, 8
	s_add_i32 s35, 0, 0x14000
	v_lshlrev_b32_e32 v68, 2, v92
	s_lshl_b32 s34, s49, 6
	s_lshl_b32 s96, s49, 7
	v_bfi_b32 v42, -16, s2, v35
	s_add_i32 s2, s3, 64
	s_add_i32 s51, s35, s9
	v_lshl_add_u64 v[94:95], s[0:1], 0, v[68:69]
	s_lshl_b64 s[0:1], s[4:5], 10
	s_add_u32 s0, s38, s0
	v_lshlrev_b32_e32 v68, 4, v67
	s_addc_u32 s1, s39, s1
	s_movk_i32 s36, 0x48
	v_lshl_add_u64 v[44:45], s[0:1], 0, v[68:69]
	s_mov_b64 s[0:1], 0x5f17a100
	v_mul_f32_e32 v34, 0x4f7ffffe, v34
	v_lshrrev_b32_e32 v46, 4, v67
	v_mul_lo_u32 v47, v42, s36
	v_or_b32_e32 v42, s2, v43
	v_lshl_add_u64 v[96:97], v[44:45], 0, s[0:1]
	v_and_or_b32 v44, s8, 32, v43
	v_cvt_u32_f32_e32 v34, v34
	v_and_b32_e32 v38, 7, v35
	v_ashrrev_i32_e32 v106, 4, v35
	v_mul_lo_u32 v49, v42, s36
	v_lshl_or_b32 v51, v46, 2, s3
	v_and_b32_e32 v42, 48, v35
	v_mul_lo_u32 v35, v40, s11
	v_lshlrev_b64 v[40:41], 7, v[40:41]
	v_or_b32_e32 v79, 16, v44
	v_lshlrev_b32_e32 v48, 3, v46
	v_lshl_add_u64 v[40:41], s[6:7], 0, v[40:41]
	v_cmp_gt_i32_e64 s[4:5], v44, v51
	v_cmp_lt_i32_e64 s[6:7], v44, v51
	v_mul_lo_u32 v56, v51, s11
	v_or_b32_e32 v57, 1, v51
	v_or_b32_e32 v68, 2, v51
	v_or_b32_e32 v78, 3, v51
	v_cmp_gt_i32_e64 s[18:19], v79, v51
	v_cmp_lt_i32_e64 s[20:21], v79, v51
	v_lshlrev_b32_e32 v51, 1, v79
	v_mad_u32_u24 v105, v67, s11, v36
	v_or_b32_e32 v50, 0x1200, v48
	v_cmp_eq_u32_e64 s[2:3], 0, v43
	v_mul_u32_u24_e32 v45, 0x48, v44
	v_lshl_add_u32 v55, v44, 1, s92
	v_cmp_gt_i32_e64 s[8:9], v44, v57
	v_cmp_gt_i32_e64 s[10:11], v44, v68
	v_cmp_lt_i32_e64 s[12:13], v44, v68
	v_cmp_gt_i32_e64 s[14:15], v44, v78
	v_cmp_lt_i32_e64 s[16:17], v44, v78
	v_mad_u32_u24 v44, v44, s36, v240
	v_add3_u32 v108, s92, v56, v51
	v_cmp_gt_i32_e64 s[22:23], v79, v57
	v_cmp_gt_i32_e64 s[24:25], v79, v68
	v_cmp_lt_i32_e64 s[26:27], v79, v68
	v_mul_u32_u24_e32 v51, 0x48, v43
	v_mad_u32_u24 v57, v43, s36, v240
	v_mad_u32_u24 v68, v43, s36, v241
	v_mad_u32_u24 v43, v43, s36, v242
	s_movk_i32 s0, 0x88
	v_add_lshl_u32 v47, v47, v48, 1
	v_add_lshl_u32 v54, v45, v48, 1
	v_add_lshl_u32 v49, v49, v48, 1
	v_add_lshl_u32 v80, v44, v48, 1
	v_add_lshl_u32 v112, v48, v51, 1
	v_add_lshl_u32 v113, v57, v48, 1
	v_add_lshl_u32 v114, v68, v48, 1
	v_add_lshl_u32 v115, v43, v48, 1
	v_add_lshl_u32 v48, v50, v43, 1
	v_mul_lo_u32 v43, v106, s0
	s_sub_i32 s56, 0, s45
	v_readfirstlane_b32 s0, v34
	s_mul_i32 s1, s56, s0
	s_mul_hi_u32 s1, s0, s1
	s_add_i32 s57, s0, s1
	s_lshl_b32 s0, s49, 8
	s_add_u32 s0, s40, s0
	v_cmp_gt_i32_e64 s[28:29], v79, v78
	v_cmp_lt_i32_e64 s[30:31], v79, v78
	v_add_lshl_u32 v78, v50, v68, 1
	s_addc_u32 s1, s41, 0
	v_lshlrev_b32_e32 v68, 1, v92
	v_lshlrev_b32_e32 v36, 3, v38
	v_lshlrev_b32_e32 v38, 4, v38
	v_add_u32_e32 v52, 0, v42
	v_add_lshl_u32 v45, v45, v50, 1
	v_add_lshl_u32 v44, v44, v50, 1
	v_add_lshl_u32 v51, v50, v51, 1
	v_add_lshl_u32 v57, v50, v57, 1
	v_mul_u32_u24_e32 v46, 0x440, v46
	v_add_lshl_u32 v117, v43, v92, 1
	v_lshl_add_u64 v[98:99], s[0:1], 0, v[68:69]
	v_mov_b32_e32 v43, v69
	s_lshl_b32 s0, s45, 12
	v_add_u32_e32 v107, 32, v106
	v_lshl_add_u64 v[100:101], v[40:41], 0, v[42:43]
	s_lshl_b32 s36, s45, 6
	s_sub_i32 s37, 0, s0
	s_add_i32 s0, s84, s44
	v_add_u32_e32 v120, v37, v39
	v_lshlrev_b32_e32 v68, 1, v36
	v_lshlrev_b32_e32 v102, 1, v38
	v_add_u32_e32 v121, 0, v47
	v_add_u32_e32 v122, 0, v54
	v_add_u32_e32 v123, 0, v49
	v_add_u32_e32 v124, 0, v45
	v_add_u32_e32 v125, v55, v56
	v_add_u32_e32 v127, 0, v44
	v_add_u32_e32 v128, v52, v35
	v_add_u32_e32 v129, 0, v51
	v_add_u32_e32 v130, 0, v57
	v_add_u32_e32 v132, 0, v48
	v_add_u32_e32 v133, v53, v46
	s_waitcnt vmcnt(2)
	v_mov_b64_e32 v[54:55], v[62:63]
	v_mov_b64_e32 v[46:47], v[74:75]
	v_mov_b64_e32 v[50:51], v[58:59]
	v_mov_b64_e32 v[38:39], v[70:71]
	v_mov_b64_e32 v[44:45], v[20:21]
	v_mov_b64_e32 v[36:37], v[24:25]
	s_mov_b32 s97, s67
	v_mov_b32_e32 v93, v69
	v_add_u32_e32 v109, 0x90, v108
	v_add_u32_e32 v110, 0x120, v108
	v_add_u32_e32 v111, 0x1b0, v108
	v_lshl_add_u32 v116, v106, 2, s35
	v_lshl_add_u32 v118, v107, 2, s35
	v_add_u32_e32 v119, 0x2200, v117
	s_lshl_b32 s71, s44, 6
	s_lshl_b32 s74, s84, 6
	s_sub_i32 s75, 0, s36
	s_lshl_b32 s79, s44, 12
	s_lshl_b32 s80, s84, 12
	s_sub_i32 s81, 0xffffffc0, s0
	s_lshl_b32 s66, s34, 1
	v_add_u32_e32 v126, 0, v80
	v_add_u32_e32 v131, 0, v78
	v_mov_b64_e32 v[56:57], v[64:65]
	v_mov_b64_e32 v[48:49], v[76:77]
	v_mov_b64_e32 v[52:53], v[60:61]
	v_mov_b64_e32 v[40:41], v[72:73]
	v_mov_b64_e32 v[42:43], v[18:19]
	v_mov_b64_e32 v[34:35], v[22:23]
	s_waitcnt vmcnt(0)
	v_readfirstlane_b32 vcc_lo, v0
	s_nop 3
	s_and_b32 vcc_lo, vcc_lo, 0x3ff
	s_lshr_b32 vcc_lo, vcc_lo, 6
	s_cmp_ge_u32 vcc_lo, 4
	s_cbranch_scc1 .Lprio_done_c3
	s_setprio 1
.Lprio_done_c3:
	s_branch .LBB0_661
.LBB0_660:
	s_or_b64 exec, exec, s[0:1]
	s_ashr_i32 s0, s84, 31
	v_cvt_pk_bf16_f32 v58, v61, s0
	ds_write_b16 v133, v58 offset:13872
	s_waitcnt lgkmcnt(0)
	s_barrier
	global_load_dwordx4 v[58:61], v[94:95], off offset:16
	global_load_dwordx4 v[62:65], v[94:95], off
	s_abs_i32 s1, s84
	s_mul_hi_u32 s34, s1, s57
	s_mul_i32 s35, s34, s45
	s_sub_i32 s1, s1, s35
	s_add_i32 s35, s34, 1
	s_sub_i32 s50, s1, s45
	s_cmp_ge_u32 s1, s45
	s_cselect_b32 s34, s35, s34
	s_cselect_b32 s1, s50, s1
	s_add_i32 s35, s34, 1
	s_cmp_ge_u32 s1, s45
	s_cselect_b32 s1, s35, s34
	s_xor_b32 s1, s1, s0
	s_sub_i32 s35, s1, s0
	s_mul_i32 s34, s56, s35
	s_add_i32 s50, s65, s34
	s_lshl_b32 s1, s1, 8
	s_mul_i32 s34, s36, s35
	s_sub_i32 s1, s1, s34
	s_lshl_b32 s0, s0, 8
	s_sub_i32 s0, s1, s0
	s_add_i32 s1, s71, s74
	s_add_i32 s34, s1, s0
	s_mul_i32 s0, s37, s35
	s_add_i32 s69, s79, s80
	s_add_i32 s69, s69, s0
	s_and_b32 s0, s69, 0x1000
	s_add_i32 s69, s50, -4
	s_lshr_b32 s69, s69, 1
	s_add_i32 s69, s69, s0
	s_mul_i32 s0, s75, s35
	v_and_b32_e32 v136, 0xffff0000, v23
	s_add_i32 s0, s1, s0
	v_lshlrev_b32_e32 v134, 16, v23
	v_mul_f32_e32 v23, 0xbfb8aa3b, v136
	s_lshl_b32 s65, s35, 13
	s_add_i32 s35, s0, 0xffffff00
	v_exp_f32_e32 v23, v23
	s_and_b64 s[0:1], s[94:95], exec
	s_cselect_b32 s0, s69, s35
	s_add_i32 s35, s0, s65
	s_add_i32 s65, 0, 0x14800
	v_add_u32_e32 v70, s65, v117
	v_add_f32_e32 v23, 1.0, v23
	v_lshlrev_b32_e32 v142, 16, v24
	ds_read_b128 v[82:85], v70
	ds_read2st64_b32 v[86:87], v116 offset1:1
	ds_read2st64_b32 v[80:81], v116 offset0:2 offset1:3
	ds_read2st64_b32 v[78:79], v116 offset0:4 offset1:5
	ds_read2st64_b32 v[76:77], v116 offset0:6 offset1:7
	v_rcp_f32_e32 v140, v23
	v_mul_f32_e32 v23, 0xbfb8aa3b, v142
	v_and_b32_e32 v144, 0xffff0000, v24
	ds_read2st64_b32 v[156:157], v118 offset1:1
	v_exp_f32_e32 v23, v23
	v_mul_f32_e32 v24, 0xbfb8aa3b, v144
	s_waitcnt lgkmcnt(5)
	v_lshlrev_b32_e32 v135, 16, v83
	v_and_b32_e32 v137, 0xffff0000, v83
	v_exp_f32_e32 v83, v24
	v_add_u32_e32 v70, s65, v119
	ds_read_b128 v[70:73], v70
	ds_read2st64_b32 v[158:159], v118 offset0:2 offset1:3
	ds_read2st64_b32 v[160:161], v118 offset0:4 offset1:5
	ds_read2st64_b32 v[162:163], v118 offset0:6 offset1:7
	v_add_f32_e32 v23, 1.0, v23
	s_waitcnt lgkmcnt(4)
	v_mov_b32_e32 v164, v156
	v_mov_b32_e32 v165, v86
	v_rcp_f32_e32 v24, v23
	v_add_f32_e32 v23, 1.0, v83
	v_lshlrev_b32_e32 v146, 16, v25
	v_pk_add_f32 v[164:165], v[164:165], 0 op_sel_hi:[1,0]
	v_mov_b32_e32 v86, v157
	s_addk_i32 s35, 0x400
	v_lshlrev_b32_e32 v143, 16, v84
	v_and_b32_e32 v145, 0xffff0000, v84
	v_rcp_f32_e32 v84, v23
	v_mul_f32_e32 v23, 0xbfb8aa3b, v146
	v_and_b32_e32 v148, 0xffff0000, v25
	v_pk_add_f32 v[86:87], v[164:165], v[86:87]
	s_waitcnt lgkmcnt(2)
	v_mov_b32_e32 v156, v158
	v_mov_b32_e32 v157, v80
	s_cmp_gt_i32 s50, 3
	v_exp_f32_e32 v23, v23
	v_mul_f32_e32 v25, 0xbfb8aa3b, v148
	v_pk_add_f32 v[86:87], v[86:87], v[156:157]
	v_mov_b32_e32 v80, v159
	s_cselect_b64 s[0:1], -1, 0
	v_lshlrev_b32_e32 v74, 16, v22
	v_exp_f32_e32 v25, v25
	v_pk_add_f32 v[80:81], v[86:87], v[80:81]
	s_waitcnt lgkmcnt(1)
	v_mov_b32_e32 v86, v160
	v_mov_b32_e32 v87, v78
	v_mul_f32_e32 v88, 0xbfb8aa3b, v74
	s_and_b64 s[88:89], s[0:1], exec
	v_pk_add_f32 v[80:81], v[80:81], v[86:87]
	v_mov_b32_e32 v78, v161
	v_exp_f32_e32 v89, v88
	v_and_b32_e32 v88, 0xffff0000, v22
	s_cselect_b32 s34, s35, s34
	s_and_b64 s[0:1], s[0:1], s[94:95]
	v_pk_add_f32 v[78:79], v[80:81], v[78:79]
	s_waitcnt lgkmcnt(0)
	v_mov_b32_e32 v80, v162
	v_mov_b32_e32 v81, v76
	v_mul_f32_e32 v22, 0xbfb8aa3b, v88
	v_add_f32_e32 v23, 1.0, v23
	s_and_b64 s[0:1], s[0:1], exec
	v_pk_add_f32 v[78:79], v[78:79], v[80:81]
	v_mov_b32_e32 v76, v163
	v_exp_f32_e32 v103, v22
	v_rcp_f32_e32 v150, v23
	v_add_f32_e32 v23, 1.0, v25
	s_cselect_b32 s0, 6, 0
	v_pk_add_f32 v[76:77], v[78:79], v[76:77]
	s_brev_b32 s50, 60
	v_rcp_f32_e32 v152, v23
	v_lshlrev_b32_e32 v23, s0, v106
	v_pk_fma_f32 v[76:77], v[76:77], s[50:51], v[198:199] op_sel_hi:[1,0,0]
	v_add_u32_e32 v154, s34, v23
	v_mul_f32_e32 v23, 0x4b800000, v77
	v_cmp_gt_f32_e32 vcc, s93, v77
	v_lshlrev_b32_e32 v75, 16, v82
	v_add_f32_e32 v22, 1.0, v89
	v_cndmask_b32_e32 v23, v77, v23, vcc
	v_and_b32_e32 v89, 0xffff0000, v82
	v_add_f32_e32 v82, 1.0, v103
	v_mul_f32_e32 v103, 0xbfb8aa3b, v134
	v_rsq_f32_e32 v23, v23
	v_exp_f32_e32 v103, v103
	v_rcp_f32_e32 v22, v22
	v_rcp_f32_e32 v82, v82
	v_mul_f32_e32 v25, 0x45800000, v23
	v_add_f32_e32 v103, 1.0, v103
	v_cndmask_b32_e32 v23, v23, v25, vcc
	v_rcp_f32_e32 v138, v103
	v_pk_mul_f32 v[74:75], v[22:23], v[74:75]
	v_mov_b32_e32 v83, v23
	s_waitcnt vmcnt(0)
	v_mul_f32_e32 v22, v62, v75
	v_mul_f32_e32 v77, v74, v22
	v_pk_mul_f32 v[74:75], v[82:83], v[88:89]
	v_mov_b32_e32 v139, v23
	v_mul_f32_e32 v22, v63, v75
	v_mul_f32_e32 v80, v74, v22
	v_pk_mul_f32 v[74:75], v[138:139], v[134:135]
	v_mov_b32_e32 v141, v23
	v_mul_f32_e32 v22, v64, v75
	v_mul_f32_e32 v81, v74, v22
	v_pk_mul_f32 v[74:75], v[140:141], v[136:137]
	v_mov_b32_e32 v25, v23
	v_mul_f32_e32 v22, v65, v75
	v_pk_mul_f32 v[24:25], v[24:25], v[142:143]
	v_lshlrev_b32_e32 v147, 16, v85
	v_and_b32_e32 v149, 0xffff0000, v85
	v_mul_f32_e32 v74, v74, v22
	v_mul_f32_e32 v22, v58, v25
	v_mov_b32_e32 v85, v23
	v_mul_f32_e32 v75, v24, v22
	v_pk_mul_f32 v[24:25], v[84:85], v[144:145]
	v_mov_b32_e32 v151, v23
	v_mul_f32_e32 v22, v59, v25
	v_mul_f32_e32 v82, v24, v22
	v_pk_mul_f32 v[24:25], v[150:151], v[146:147]
	v_mov_b32_e32 v153, v23
	v_mul_f32_e32 v22, v60, v25
	v_mul_f32_e32 v83, v24, v22
	v_mov_b32_e32 v24, v69
	v_mov_b32_e32 v25, v69
	v_cvt_pk_fp8_f32 v24, v77, v80
	v_cvt_pk_fp8_f32 v25, v75, v82
	v_ashrrev_i32_e32 v155, 31, v154
	v_pk_mul_f32 v[22:23], v[152:153], v[148:149]
	v_lshlrev_b64 v[154:155], 10, v[154:155]
	v_mul_f32_e32 v23, v61, v23
	v_lshl_add_u64 v[78:79], s[38:39], 0, v[154:155]
	v_mul_f32_e32 v22, v22, v23
	v_lshl_add_u64 v[78:79], v[78:79], 0, s[96:97]
	v_cvt_pk_fp8_f32 v24, v81, v74 op_sel:[0,0,1]
	v_cvt_pk_fp8_f32 v25, v83, v22 op_sel:[0,0,1]
	v_lshl_add_u64 v[78:79], v[78:79], 0, v[92:93]
	s_mov_b32 s1, 0x56d7a000
	v_add_co_u32_e32 v22, vcc, s1, v78
	v_and_b32_e32 v74, 0xffff0000, v18
	s_nop 0
	v_addc_co_u32_e32 v23, vcc, 0, v79, vcc
	global_store_dwordx2 v[22:23], v[24:25], off offset:768
	v_mul_f32_e32 v22, 0x4b800000, v76
	v_cmp_gt_f32_e32 vcc, s93, v76
	v_and_b32_e32 v75, 0xffff0000, v70
	s_addk_i32 s74, 0x1000
	v_cndmask_b32_e32 v22, v76, v22, vcc
	v_rsq_f32_e32 v23, v22
	v_lshlrev_b32_e32 v22, 16, v18
	v_mul_f32_e32 v24, 0xbfb8aa3b, v22
	v_exp_f32_e32 v24, v24
	v_mul_f32_e32 v18, 0xbfb8aa3b, v74
	v_exp_f32_e32 v18, v18
	v_mul_f32_e32 v25, 0x45800000, v23
	v_add_f32_e32 v24, 1.0, v24
	v_rcp_f32_e32 v24, v24
	v_cndmask_b32_e32 v25, v23, v25, vcc
	v_lshlrev_b32_e32 v23, 16, v70
	v_add_f32_e32 v18, 1.0, v18
	v_pk_mul_f32 v[22:23], v[24:25], v[22:23]
	v_rcp_f32_e32 v24, v18
	v_mul_f32_e32 v23, v62, v23
	v_lshlrev_b32_e32 v18, 16, v19
	v_mul_f32_e32 v76, v22, v23
	v_mul_f32_e32 v22, 0xbfb8aa3b, v18
	v_exp_f32_e32 v62, v22
	v_pk_mul_f32 v[22:23], v[24:25], v[74:75]
	s_add_i32 s80, s80, 0x40000
	v_mul_f32_e32 v23, v63, v23
	v_add_f32_e32 v24, 1.0, v62
	v_and_b32_e32 v62, 0xffff0000, v19
	v_mul_f32_e32 v19, 0xbfb8aa3b, v62
	v_exp_f32_e32 v63, v19
	v_rcp_f32_e32 v24, v24
	v_mul_f32_e32 v70, v22, v23
	v_lshlrev_b32_e32 v19, 16, v71
	v_add_f32_e32 v22, 1.0, v63
	v_pk_mul_f32 v[18:19], v[24:25], v[18:19]
	v_rcp_f32_e32 v24, v22
	v_lshlrev_b32_e32 v22, 16, v20
	v_mul_f32_e32 v19, v64, v19
	v_and_b32_e32 v63, 0xffff0000, v71
	v_mul_f32_e32 v23, 0xbfb8aa3b, v22
	v_mul_f32_e32 v64, v18, v19
	v_pk_mul_f32 v[18:19], v[24:25], v[62:63]
	v_exp_f32_e32 v24, v23
	v_mul_f32_e32 v19, v65, v19
	v_mul_f32_e32 v62, v18, v19
	v_lshlrev_b32_e32 v23, 16, v72
	v_add_f32_e32 v18, 1.0, v24
	v_rcp_f32_e32 v24, v18
	v_and_b32_e32 v18, 0xffff0000, v20
	v_mul_f32_e32 v19, 0xbfb8aa3b, v18
	v_exp_f32_e32 v19, v19
	v_pk_mul_f32 v[22:23], v[24:25], v[22:23]
	s_sub_i32 s81, s81, 64
	v_mul_f32_e32 v20, v58, v23
	v_mul_f32_e32 v58, v22, v20
	v_add_f32_e32 v19, 1.0, v19
	v_lshlrev_b32_e32 v20, 16, v21
	v_rcp_f32_e32 v24, v19
	v_mul_f32_e32 v19, 0xbfb8aa3b, v20
	v_exp_f32_e32 v22, v19
	v_and_b32_e32 v19, 0xffff0000, v72
	v_pk_mul_f32 v[18:19], v[24:25], v[18:19]
	s_mov_b32 s84, s85
	v_add_f32_e32 v22, 1.0, v22
	v_rcp_f32_e32 v24, v22
	v_and_b32_e32 v22, 0xffff0000, v21
	v_mul_f32_e32 v21, 0xbfb8aa3b, v22
	v_exp_f32_e32 v23, v21
	v_mul_f32_e32 v19, v59, v19
	v_lshlrev_b32_e32 v21, 16, v73
	v_mul_f32_e32 v59, v18, v19
	v_pk_mul_f32 v[18:19], v[24:25], v[20:21]
	v_add_f32_e32 v20, 1.0, v23
	v_rcp_f32_e32 v24, v20
	v_mov_b32_e32 v21, v69
	v_mul_f32_e32 v19, v60, v19
	v_and_b32_e32 v23, 0xffff0000, v73
	v_cvt_pk_fp8_f32 v21, v58, v59
	v_mul_f32_e32 v60, v18, v19
	v_pk_mul_f32 v[18:19], v[24:25], v[22:23]
	v_mov_b32_e32 v20, v69
	v_mul_f32_e32 v19, v61, v19
	v_mul_f32_e32 v18, v18, v19
	v_cvt_pk_fp8_f32 v21, v60, v18 op_sel:[0,0,1]
	v_lshlrev_b32_e32 v18, s0, v107
	v_cvt_pk_fp8_f32 v20, v76, v70
	v_add_u32_e32 v18, s34, v18
	v_ashrrev_i32_e32 v19, 31, v18
	v_lshlrev_b64 v[18:19], 10, v[18:19]
	v_lshl_add_u64 v[18:19], s[38:39], 0, v[18:19]
	v_cvt_pk_fp8_f32 v20, v64, v62 op_sel:[0,0,1]
	v_lshl_add_u64 v[18:19], v[18:19], 0, s[96:97]
	v_lshl_add_u64 v[18:19], v[18:19], 0, v[92:93]
	v_add_co_u32_e32 v18, vcc, 0x56d7a000, v18
	v_mov_b64_e32 v[64:65], v[56:57]
	s_nop 0
	v_addc_co_u32_e32 v19, vcc, 0, v19, vcc
	global_store_dwordx2 v[18:19], v[20:21], off offset:768
	v_mov_b64_e32 v[76:77], v[48:49]
	v_mov_b64_e32 v[60:61], v[52:53]
	v_mov_b64_e32 v[72:73], v[40:41]
	v_mov_b64_e32 v[18:19], v[42:43]
	v_mov_b64_e32 v[22:23], v[34:35]
	s_andn2_b64 vcc, exec, s[86:87]
	v_mov_b64_e32 v[62:63], v[54:55]
	v_mov_b64_e32 v[74:75], v[46:47]
	v_mov_b64_e32 v[58:59], v[50:51]
	v_mov_b64_e32 v[70:71], v[38:39]
	v_mov_b64_e32 v[20:21], v[44:45]
	v_mov_b64_e32 v[24:25], v[36:37]
	s_cbranch_vccz .LBB0_708

.LBB0_708:
	s_setprio 0
	v_readlane_b32 s86, v247, 26
	v_readlane_b32 s95, v247, 24
	v_readlane_b32 s85, v247, 25
	v_readlane_b32 s87, v247, 27
	s_movk_i32 s94, 0x6000
